# baseline (speedup 1.0000x reference)
.Lmy_noperm_in:
	s_cmp_gt_u32 s35, 0xff
	s_cbranch_scc0 .Lmy_prio_done
	s_setprio 1
